# grid barrier early L2 write-back at the 17th, 25th and 29th arrivals of each XCD (was 17th and 25th)
# baseline (speedup 1.0000x reference)
.LBB0_73:
	s_or_b64 exec, exec, s[12:13]
	v_cvt_f32_u32_e32 v5, v3
	s_waitcnt vmcnt(0)
	v_readfirstlane_b32 s0, v4
	v_sub_u32_e32 v4, 0, v3
	v_rcp_iflag_f32_e32 v5, v5
	v_add_u32_e32 v6, s0, v2
	v_mul_f32_e32 v5, 0x4f7ffffe, v5
	v_cvt_u32_f32_e32 v5, v5
	v_mul_lo_u32 v2, v4, v5
	v_mul_hi_u32 v2, v5, v2
	v_add_u32_e32 v2, v5, v2
	v_mul_hi_u32 v2, v6, v2
	v_mul_lo_u32 v4, v2, v3
	v_sub_u32_e32 v4, v6, v4
	v_add_u32_e32 v5, 1, v2
	v_cmp_ge_u32_e32 vcc, v4, v3
	s_nop 1
	v_cndmask_b32_e32 v2, v2, v5, vcc
	v_sub_u32_e32 v5, v4, v3
	v_cndmask_b32_e32 v4, v4, v5, vcc
	v_add_u32_e32 v5, 1, v2
	v_cmp_ge_u32_e32 vcc, v4, v3
	v_add_u32_e32 v4, 1, v6
	s_nop 0
	v_cndmask_b32_e32 v2, v2, v5, vcc
	v_mul_lo_u32 v5, v3, v2
	v_add_u32_e32 v3, v5, v3
	v_cmp_ne_u32_e32 vcc, v4, v3
	s_and_saveexec_b64 s[0:1], vcc
	s_xor_b64 s[10:11], exec, s[0:1]
	s_cbranch_execz .LBB0_87
	v_readfirstlane_b32 s0, v6
	v_readfirstlane_b32 s1, v5
	v_readfirstlane_b32 vcc_lo, v3
	s_nop 3
	s_sub_u32 s0, s0, s1
	s_sub_u32 s1, vcc_lo, s1
	s_lshr_b32 vcc_lo, s1, 1
	s_cmp_eq_u32 s0, vcc_lo
	s_cbranch_scc1 .Lpf_do_0
	s_lshr_b32 vcc_lo, s1, 3
	s_sub_u32 vcc_lo, s1, vcc_lo
	s_cmp_eq_u32 s0, vcc_lo
	s_cbranch_scc1 .Lpf_do_0
	s_mul_i32 s1, s1, 3
	s_lshr_b32 s1, s1, 2
	s_cmp_lg_u32 s0, s1
	s_cbranch_scc1 .Lpf_skip_0

.LBB0_2258:
	s_or_b64 exec, exec, s[10:11]
	v_cvt_f32_u32_e32 v5, v3
	s_waitcnt vmcnt(0)
	v_readfirstlane_b32 s0, v4
	v_sub_u32_e32 v4, 0, v3
	v_rcp_iflag_f32_e32 v5, v5
	v_add_u32_e32 v6, s0, v2
	v_mul_f32_e32 v5, 0x4f7ffffe, v5
	v_cvt_u32_f32_e32 v5, v5
	v_mul_lo_u32 v2, v4, v5
	v_mul_hi_u32 v2, v5, v2
	v_add_u32_e32 v2, v5, v2
	v_mul_hi_u32 v2, v6, v2
	v_mul_lo_u32 v4, v2, v3
	v_sub_u32_e32 v4, v6, v4
	v_add_u32_e32 v5, 1, v2
	v_cmp_ge_u32_e32 vcc, v4, v3
	s_nop 1
	v_cndmask_b32_e32 v2, v2, v5, vcc
	v_sub_u32_e32 v5, v4, v3
	v_cndmask_b32_e32 v4, v4, v5, vcc
	v_add_u32_e32 v5, 1, v2
	v_cmp_ge_u32_e32 vcc, v4, v3
	v_add_u32_e32 v4, 1, v6
	s_nop 0
	v_cndmask_b32_e32 v2, v2, v5, vcc
	v_mul_lo_u32 v5, v3, v2
	v_add_u32_e32 v3, v5, v3
	v_cmp_ne_u32_e32 vcc, v4, v3
	s_and_saveexec_b64 s[0:1], vcc
	s_xor_b64 s[8:9], exec, s[0:1]
	s_cbranch_execz .LBB0_2272
	v_readfirstlane_b32 s0, v6
	v_readfirstlane_b32 s1, v5
	v_readfirstlane_b32 vcc_lo, v3
	s_nop 3
	s_sub_u32 s0, s0, s1
	s_sub_u32 s1, vcc_lo, s1
	s_lshr_b32 vcc_lo, s1, 1
	s_cmp_eq_u32 s0, vcc_lo
	s_cbranch_scc1 .Lpf_do_17
	s_lshr_b32 vcc_lo, s1, 3
	s_sub_u32 vcc_lo, s1, vcc_lo
	s_cmp_eq_u32 s0, vcc_lo
	s_cbranch_scc1 .Lpf_do_17
	s_mul_i32 s1, s1, 3
	s_lshr_b32 s1, s1, 2
	s_cmp_lg_u32 s0, s1
	s_cbranch_scc1 .Lpf_skip_17
